# E row loop: nt loads for the f32 residual rows too
# speedup vs baseline: 1.0204x; 1.0051x over previous
.LBB0_948:
	global_load_dwordx4 v[64:67], v[68:69], off offset:2064 nt

.LBB0_966:
	global_load_dwordx4 v[52:55], v[68:69], off nt
	s_and_b64 vcc, exec, s[40:41]
	v_mov_b64_e32 v[58:59], v[160:161]
	v_mov_b64_e32 v[56:57], v[158:159]
	s_cbranch_vccnz .LBB0_946
.LBB0_967:
	global_load_dwordx4 v[56:59], v[68:69], off offset:16 nt
	s_and_b64 vcc, exec, s[40:41]
	v_mov_b64_e32 v[62:63], v[156:157]
	v_mov_b64_e32 v[60:61], v[154:155]
	s_cbranch_vccnz .LBB0_947
.LBB0_968:
	global_load_dwordx4 v[60:63], v[68:69], off offset:2048 nt
	s_and_b64 vcc, exec, s[40:41]
	v_mov_b64_e32 v[66:67], v[152:153]
	v_mov_b64_e32 v[64:65], v[150:151]
	s_cbranch_vccz .LBB0_948
	s_branch .LBB0_949
